# accumulator zero-fill of the P1/P3/P4 GEMM units with 64-bit moves (64 instead of 128 VALU ops per wave per unit)
# speedup vs baseline: 1.0123x; 1.0021x over previous
.LBB0_326:
	v_readlane_b32 s0, v255, 48
	v_readlane_b32 s1, v255, 49
	s_andn2_b64 vcc, exec, s[0:1]
	v_mov_b32_e32 v37, 0
	s_cbranch_vccnz .LBB0_349
	s_lshl_b32 s0, s93, 10
	s_and_b32 s2, s0, 0x400
	s_cmp_eq_u32 s30, 0
	s_cselect_b32 s0, s67, s96
	s_ashr_i32 s1, s0, 31
	s_cmp_eq_u32 s94, 2
	s_cselect_b32 s3, 3, 7
	s_cmp_lg_u32 s94, 1
	s_cselect_b32 s3, s3, 1
	s_lshl_b32 s3, s76, s3
	s_lshl_b32 s11, s3, 1
	s_lshl_b64 s[0:1], s[0:1], 2
	s_add_u32 s0, s18, s0
	s_addc_u32 s1, s19, s1
	s_add_u32 s28, s28, 0x80
	s_addc_u32 s29, s29, 0
	v_writelane_b32 v255, s30, 60
	s_add_u32 s30, s60, 0x100
	s_addc_u32 s31, s61, 0
	v_mov_b64_e32 v[34:35], 0
	v_mov_b64_e32 v[36:37], 0
	v_mov_b64_e32 v[38:39], 0
	v_mov_b64_e32 v[40:41], 0
	v_mov_b64_e32 v[42:43], 0
	v_mov_b64_e32 v[44:45], 0
	v_mov_b64_e32 v[46:47], 0
	v_mov_b64_e32 v[48:49], 0
	v_mov_b64_e32 v[50:51], 0
	v_mov_b64_e32 v[52:53], 0
	v_mov_b64_e32 v[54:55], 0
	v_mov_b64_e32 v[56:57], 0
	v_mov_b64_e32 v[58:59], 0
	v_mov_b64_e32 v[60:61], 0
	v_mov_b64_e32 v[62:63], 0
	v_mov_b64_e32 v[64:65], 0
	v_mov_b64_e32 v[66:67], 0
	v_mov_b64_e32 v[68:69], 0
	v_mov_b64_e32 v[70:71], 0
	v_mov_b64_e32 v[72:73], 0
	v_mov_b64_e32 v[74:75], 0
	v_mov_b64_e32 v[76:77], 0
	v_mov_b64_e32 v[78:79], 0
	v_mov_b64_e32 v[80:81], 0
	v_mov_b64_e32 v[82:83], 0
	v_mov_b64_e32 v[84:85], 0
	v_mov_b64_e32 v[86:87], 0
	v_mov_b64_e32 v[88:89], 0
	v_mov_b64_e32 v[90:91], 0
	v_mov_b64_e32 v[92:93], 0
	v_mov_b64_e32 v[94:95], 0
	v_mov_b64_e32 v[96:97], 0
	v_mov_b64_e32 v[98:99], 0
	v_mov_b64_e32 v[100:101], 0
	v_mov_b64_e32 v[102:103], 0
	v_mov_b64_e32 v[104:105], 0
	v_mov_b64_e32 v[106:107], 0
	v_mov_b64_e32 v[108:109], 0
	v_mov_b64_e32 v[110:111], 0
	v_mov_b64_e32 v[112:113], 0
	v_mov_b64_e32 v[114:115], 0
	v_mov_b64_e32 v[116:117], 0
	v_mov_b64_e32 v[118:119], 0
	v_mov_b64_e32 v[120:121], 0
	v_mov_b64_e32 v[122:123], 0
	v_mov_b64_e32 v[124:125], 0
	v_mov_b64_e32 v[126:127], 0
	v_mov_b64_e32 v[128:129], 0
	v_mov_b64_e32 v[130:131], 0
	v_mov_b64_e32 v[132:133], 0
	v_mov_b64_e32 v[134:135], 0
	v_mov_b64_e32 v[136:137], 0
	v_mov_b64_e32 v[138:139], 0
	v_mov_b64_e32 v[140:141], 0
	v_mov_b64_e32 v[142:143], 0
	v_mov_b64_e32 v[144:145], 0
	v_mov_b64_e32 v[146:147], 0
	v_mov_b64_e32 v[148:149], 0
	v_mov_b64_e32 v[150:151], 0
	v_mov_b64_e32 v[152:153], 0
	v_mov_b64_e32 v[154:155], 0
	v_mov_b64_e32 v[156:157], 0
	v_mov_b64_e32 v[158:159], 0
	v_mov_b64_e32 v[160:161], 0
	s_add_i32 s82, s2, 0
	s_mov_b32 s10, 0
	s_add_i32 s82, s82, 0x21000
	s_branch .LBB0_331

.LBB0_888:
	v_mov_b64_e32 v[12:13], 0
	v_mov_b64_e32 v[14:15], 0
	v_mov_b64_e32 v[16:17], 0
	v_mov_b64_e32 v[18:19], 0
	v_mov_b64_e32 v[20:21], 0
	v_mov_b64_e32 v[22:23], 0
	v_mov_b64_e32 v[24:25], 0
	v_mov_b64_e32 v[26:27], 0
	v_mov_b64_e32 v[28:29], 0
	v_mov_b64_e32 v[30:31], 0
	v_mov_b64_e32 v[32:33], 0
	v_mov_b64_e32 v[34:35], 0
	v_mov_b64_e32 v[36:37], 0
	v_mov_b64_e32 v[38:39], 0
	v_mov_b64_e32 v[40:41], 0
	v_mov_b64_e32 v[42:43], 0
	v_mov_b64_e32 v[44:45], 0
	v_mov_b64_e32 v[46:47], 0
	v_mov_b64_e32 v[48:49], 0
	v_mov_b64_e32 v[50:51], 0
	v_mov_b64_e32 v[52:53], 0
	v_mov_b64_e32 v[54:55], 0
	v_mov_b64_e32 v[56:57], 0
	v_mov_b64_e32 v[58:59], 0
	v_mov_b64_e32 v[60:61], 0
	v_mov_b64_e32 v[62:63], 0
	v_mov_b64_e32 v[64:65], 0
	v_mov_b64_e32 v[66:67], 0
	v_mov_b64_e32 v[68:69], 0
	v_mov_b64_e32 v[70:71], 0
	v_mov_b64_e32 v[72:73], 0
	v_mov_b64_e32 v[74:75], 0
	v_mov_b64_e32 v[76:77], 0
	v_mov_b64_e32 v[78:79], 0
	v_mov_b64_e32 v[80:81], 0
	v_mov_b64_e32 v[82:83], 0
	v_mov_b64_e32 v[84:85], 0
	v_mov_b64_e32 v[86:87], 0
	v_mov_b64_e32 v[88:89], 0
	v_mov_b64_e32 v[90:91], 0
	v_mov_b64_e32 v[92:93], 0
	v_mov_b64_e32 v[94:95], 0
	v_mov_b64_e32 v[96:97], 0
	v_mov_b64_e32 v[98:99], 0
	v_mov_b64_e32 v[100:101], 0
	v_mov_b64_e32 v[102:103], 0
	v_mov_b64_e32 v[104:105], 0
	v_mov_b64_e32 v[106:107], 0
	v_mov_b64_e32 v[108:109], 0
	v_mov_b64_e32 v[110:111], 0
	v_mov_b64_e32 v[112:113], 0
	v_mov_b64_e32 v[114:115], 0
	v_mov_b64_e32 v[116:117], 0
	v_mov_b64_e32 v[118:119], 0
	v_mov_b64_e32 v[120:121], 0
	v_mov_b64_e32 v[122:123], 0
	v_mov_b64_e32 v[124:125], 0
	v_mov_b64_e32 v[126:127], 0
	v_mov_b64_e32 v[128:129], 0
	v_mov_b64_e32 v[130:131], 0
	v_mov_b64_e32 v[132:133], 0
	v_mov_b64_e32 v[134:135], 0
	v_mov_b64_e32 v[136:137], 0
	v_mov_b64_e32 v[138:139], 0
	s_andn2_b64 vcc, exec, s[36:37]
	s_cbranch_vccnz .LBB0_893
	v_mov_b32_e32 v12, v10
	v_mov_b32_e32 v13, v10
	s_add_i32 s85, s83, s69
	s_add_i32 s86, s84, s72
	v_mov_b32_e32 v11, v10
	v_mov_b64_e32 v[46:47], v[12:13]
	v_mov_b64_e32 v[50:51], v[12:13]
	v_mov_b64_e32 v[62:63], v[12:13]
	v_mov_b64_e32 v[66:67], v[12:13]
	v_mov_b64_e32 v[22:23], v[12:13]
	v_mov_b64_e32 v[26:27], v[12:13]
	v_mov_b64_e32 v[38:39], v[12:13]
	v_mov_b64_e32 v[42:43], v[12:13]
	v_mov_b64_e32 v[54:55], v[12:13]
	v_mov_b64_e32 v[58:59], v[12:13]
	v_mov_b64_e32 v[70:71], v[12:13]
	v_mov_b64_e32 v[74:75], v[12:13]
	v_mov_b64_e32 v[78:79], v[12:13]
	v_mov_b64_e32 v[82:83], v[12:13]
	v_mov_b64_e32 v[94:95], v[12:13]
	v_mov_b64_e32 v[98:99], v[12:13]
	v_mov_b64_e32 v[110:111], v[12:13]
	v_mov_b64_e32 v[114:115], v[12:13]
	v_mov_b64_e32 v[126:127], v[12:13]
	v_mov_b64_e32 v[130:131], v[12:13]
	v_mov_b64_e32 v[86:87], v[12:13]
	v_mov_b64_e32 v[90:91], v[12:13]
	v_mov_b64_e32 v[102:103], v[12:13]
	v_mov_b64_e32 v[106:107], v[12:13]
	v_mov_b64_e32 v[118:119], v[12:13]
	v_mov_b64_e32 v[122:123], v[12:13]
	v_mov_b64_e32 v[134:135], v[12:13]
	v_mov_b64_e32 v[138:139], v[12:13]
	v_mov_b64_e32 v[34:35], v[12:13]
	v_mov_b64_e32 v[30:31], v[12:13]
	v_mov_b64_e32 v[18:19], v[12:13]
	s_add_u32 s87, s0, 0x100
	v_mov_b64_e32 v[44:45], v[10:11]
	v_mov_b64_e32 v[48:49], v[10:11]
	v_mov_b64_e32 v[60:61], v[10:11]
	v_mov_b64_e32 v[64:65], v[10:11]
	v_mov_b64_e32 v[20:21], v[10:11]
	v_mov_b64_e32 v[24:25], v[10:11]
	v_mov_b64_e32 v[36:37], v[10:11]
	v_mov_b64_e32 v[40:41], v[10:11]
	v_mov_b64_e32 v[52:53], v[10:11]
	v_mov_b64_e32 v[56:57], v[10:11]
	v_mov_b64_e32 v[68:69], v[10:11]
	v_mov_b64_e32 v[72:73], v[10:11]
	v_mov_b64_e32 v[76:77], v[10:11]
	v_mov_b64_e32 v[80:81], v[10:11]
	v_mov_b64_e32 v[92:93], v[10:11]
	v_mov_b64_e32 v[96:97], v[10:11]
	v_mov_b64_e32 v[108:109], v[10:11]
	v_mov_b64_e32 v[112:113], v[10:11]
	v_mov_b64_e32 v[124:125], v[10:11]
	v_mov_b64_e32 v[128:129], v[10:11]
	v_mov_b64_e32 v[84:85], v[10:11]
	v_mov_b64_e32 v[88:89], v[10:11]
	v_mov_b64_e32 v[100:101], v[10:11]
	v_mov_b64_e32 v[104:105], v[10:11]
	v_mov_b64_e32 v[116:117], v[10:11]
	v_mov_b64_e32 v[120:121], v[10:11]
	v_mov_b64_e32 v[132:133], v[10:11]
	v_mov_b64_e32 v[136:137], v[10:11]
	v_mov_b64_e32 v[32:33], v[10:11]
	v_mov_b64_e32 v[28:29], v[10:11]
	v_mov_b64_e32 v[16:17], v[10:11]
	v_mov_b64_e32 v[14:15], v[12:13]
	s_addc_u32 s88, s1, 0
	v_lshl_add_u64 v[156:157], s[52:53], 0, v[148:149]
	v_lshl_add_u64 v[158:159], s[52:53], 0, v[150:151]
	s_mov_b32 s0, 0
	s_mov_b64 s[64:65], 0
	v_mov_b64_e32 v[12:13], v[10:11]
	s_branch .LBB0_891

.LBB0_968:
	v_mov_b64_e32 v[34:35], 0
	v_mov_b64_e32 v[36:37], 0
	v_mov_b64_e32 v[38:39], 0
	v_mov_b64_e32 v[40:41], 0
	v_mov_b64_e32 v[42:43], 0
	v_mov_b64_e32 v[44:45], 0
	v_mov_b64_e32 v[46:47], 0
	v_mov_b64_e32 v[48:49], 0
	v_mov_b64_e32 v[50:51], 0
	v_mov_b64_e32 v[52:53], 0
	v_mov_b64_e32 v[54:55], 0
	v_mov_b64_e32 v[56:57], 0
	v_mov_b64_e32 v[58:59], 0
	v_mov_b64_e32 v[60:61], 0
	v_mov_b64_e32 v[62:63], 0
	v_mov_b64_e32 v[64:65], 0
	v_mov_b64_e32 v[66:67], 0
	v_mov_b64_e32 v[68:69], 0
	v_mov_b64_e32 v[70:71], 0
	v_mov_b64_e32 v[72:73], 0
	v_mov_b64_e32 v[74:75], 0
	v_mov_b64_e32 v[76:77], 0
	v_mov_b64_e32 v[78:79], 0
	v_mov_b64_e32 v[80:81], 0
	v_mov_b64_e32 v[82:83], 0
	v_mov_b64_e32 v[84:85], 0
	v_mov_b64_e32 v[86:87], 0
	v_mov_b64_e32 v[88:89], 0
	v_mov_b64_e32 v[90:91], 0
	v_mov_b64_e32 v[92:93], 0
	v_mov_b64_e32 v[94:95], 0
	v_mov_b64_e32 v[96:97], 0
	v_mov_b64_e32 v[98:99], 0
	v_mov_b64_e32 v[100:101], 0
	v_mov_b64_e32 v[102:103], 0
	v_mov_b64_e32 v[104:105], 0
	v_mov_b64_e32 v[106:107], 0
	v_mov_b64_e32 v[108:109], 0
	v_mov_b64_e32 v[110:111], 0
	v_mov_b64_e32 v[112:113], 0
	v_mov_b64_e32 v[114:115], 0
	v_mov_b64_e32 v[116:117], 0
	v_mov_b64_e32 v[118:119], 0
	v_mov_b64_e32 v[120:121], 0
	v_mov_b64_e32 v[122:123], 0
	v_mov_b64_e32 v[124:125], 0
	v_mov_b64_e32 v[126:127], 0
	v_mov_b64_e32 v[128:129], 0
	v_mov_b64_e32 v[130:131], 0
	v_mov_b64_e32 v[132:133], 0
	v_mov_b64_e32 v[134:135], 0
	v_mov_b64_e32 v[136:137], 0
	v_mov_b64_e32 v[138:139], 0
	v_mov_b64_e32 v[140:141], 0
	v_mov_b64_e32 v[142:143], 0
	v_mov_b64_e32 v[144:145], 0
	v_mov_b64_e32 v[146:147], 0
	v_mov_b64_e32 v[148:149], 0
	v_mov_b64_e32 v[150:151], 0
	v_mov_b64_e32 v[152:153], 0
	v_mov_b64_e32 v[154:155], 0
	v_mov_b64_e32 v[156:157], 0
	v_mov_b64_e32 v[158:159], 0
	v_mov_b64_e32 v[160:161], 0
	s_andn2_b64 vcc, exec, s[24:25]
	s_cbranch_vccnz .LBB0_971
	s_add_u32 s0, s0, 0x80
	s_addc_u32 s1, s1, 0
	s_add_u32 s10, s28, 0x100
	v_mov_b64_e32 v[34:35], 0
	v_mov_b64_e32 v[36:37], 0
	v_mov_b64_e32 v[38:39], 0
	v_mov_b64_e32 v[40:41], 0
	v_mov_b64_e32 v[42:43], 0
	v_mov_b64_e32 v[44:45], 0
	v_mov_b64_e32 v[46:47], 0
	v_mov_b64_e32 v[48:49], 0
	v_mov_b64_e32 v[50:51], 0
	v_mov_b64_e32 v[52:53], 0
	v_mov_b64_e32 v[54:55], 0
	v_mov_b64_e32 v[56:57], 0
	v_mov_b64_e32 v[58:59], 0
	v_mov_b64_e32 v[60:61], 0
	v_mov_b64_e32 v[62:63], 0
	v_mov_b64_e32 v[64:65], 0
	v_mov_b64_e32 v[66:67], 0
	v_mov_b64_e32 v[68:69], 0
	v_mov_b64_e32 v[70:71], 0
	v_mov_b64_e32 v[72:73], 0
	v_mov_b64_e32 v[74:75], 0
	v_mov_b64_e32 v[76:77], 0
	v_mov_b64_e32 v[78:79], 0
	v_mov_b64_e32 v[80:81], 0
	v_mov_b64_e32 v[82:83], 0
	v_mov_b64_e32 v[84:85], 0
	v_mov_b64_e32 v[86:87], 0
	v_mov_b64_e32 v[88:89], 0
	v_mov_b64_e32 v[90:91], 0
	v_mov_b64_e32 v[92:93], 0
	v_mov_b64_e32 v[94:95], 0
	v_mov_b64_e32 v[96:97], 0
	v_mov_b64_e32 v[98:99], 0
	v_mov_b64_e32 v[100:101], 0
	v_mov_b64_e32 v[102:103], 0
	v_mov_b64_e32 v[104:105], 0
	v_mov_b64_e32 v[106:107], 0
	v_mov_b64_e32 v[108:109], 0
	v_mov_b64_e32 v[110:111], 0
	v_mov_b64_e32 v[112:113], 0
	v_mov_b64_e32 v[114:115], 0
	v_mov_b64_e32 v[116:117], 0
	v_mov_b64_e32 v[118:119], 0
	v_mov_b64_e32 v[120:121], 0
	v_mov_b64_e32 v[122:123], 0
	v_mov_b64_e32 v[124:125], 0
	v_mov_b64_e32 v[126:127], 0
	v_mov_b64_e32 v[128:129], 0
	v_mov_b64_e32 v[130:131], 0
	v_mov_b64_e32 v[132:133], 0
	v_mov_b64_e32 v[134:135], 0
	v_mov_b64_e32 v[136:137], 0
	v_mov_b64_e32 v[138:139], 0
	v_mov_b64_e32 v[140:141], 0
	v_mov_b64_e32 v[142:143], 0
	v_mov_b64_e32 v[144:145], 0
	v_mov_b64_e32 v[146:147], 0
	v_mov_b64_e32 v[148:149], 0
	v_mov_b64_e32 v[150:151], 0
	v_mov_b64_e32 v[152:153], 0
	v_mov_b64_e32 v[154:155], 0
	v_mov_b64_e32 v[156:157], 0
	v_mov_b64_e32 v[158:159], 0
	v_mov_b64_e32 v[160:161], 0
	s_addc_u32 s11, s29, 0
	s_mov_b32 s28, 0
